# speedup vs baseline: 1.1028x; 1.0241x over previous
.LBB2_6:
	s_or_b64 exec, exec, s[18:19]
	v_xor_b32_e32 v23, 32, v23
	s_add_i32 s38, 0, 0x1c000
	v_lshlrev_b32_e32 v23, 2, v23
	v_lshlrev_b32_e32 v199, 2, v25
	s_waitcnt vmcnt(4) lgkmcnt(0)
	s_barrier
	v_add3_u32 v23, s38, v23, v199
	ds_read_b32 v23, v23
	v_max_f32_e32 v24, v24, v24
	v_mul_f32_e32 v22, 0x3db8aa3b, v22
	v_mov_b32_e32 v164, 0
	v_mov_b32_e32 v165, 0
	s_waitcnt lgkmcnt(0)
	s_movk_i32 s45, 0x4000
	v_add3_u32 v250, s45, v184, v185
	v_add3_u32 v251, s45, v184, v186
	v_add3_u32 v252, s45, v184, v187
	v_add3_u32 v253, s45, v184, v188
	ds_read_b128 v[218:221], v250 offset:49152
	ds_read_b128 v[222:225], v251 offset:49152
	ds_read_b128 v[242:245], v252 offset:49152
	ds_read_b128 v[246:249], v253 offset:49152
	v_add3_u32 v250, s45, v184, v189
	v_add3_u32 v251, s45, v184, v190
	v_add3_u32 v252, s45, v184, v191
	v_add3_u32 v253, s45, v184, v192
	ds_read_b128 v[202:205], v250 offset:49152
	ds_read_b128 v[206:209], v251 offset:49152
	ds_read_b128 v[210:213], v252 offset:49152
	ds_read_b128 v[214:217], v253 offset:49152
	v_max_f32_e32 v23, v23, v23
	v_max_f32_e32 v197, v24, v23
	v_mov_b32_e32 v23, 2.0
	v_fmamk_f32 v200, v197, 0xbdb8aa3b, v23
	v_fmamk_f32 v23, v22, 0xcb400000, v200
	v_fma_f32 v2, v2, v22, v23
	v_fma_f32 v3, v3, v22, v23
	v_fma_f32 v6, v6, v22, v23
	v_fma_f32 v7, v7, v22, v23
	v_fma_f32 v10, v10, v22, v23
	v_fma_f32 v11, v11, v22, v23
	v_fma_f32 v14, v14, v22, v23
	v_fma_f32 v15, v15, v22, v23
	v_exp_f32_e32 v2, v2
	v_exp_f32_e32 v3, v3
	v_exp_f32_e32 v6, v6
	v_exp_f32_e32 v7, v7
	v_exp_f32_e32 v10, v10
	v_exp_f32_e32 v11, v11
	v_exp_f32_e32 v14, v14
	v_exp_f32_e32 v15, v15
	v_fma_f32 v4, v4, v22, v23
	v_fma_f32 v5, v5, v22, v23
	v_fma_f32 v8, v8, v22, v23
	v_fma_f32 v9, v9, v22, v23
	v_fma_f32 v12, v12, v22, v23
	v_fma_f32 v13, v13, v22, v23
	v_fma_f32 v16, v16, v22, v23
	v_fmac_f32_e32 v23, v17, v22
	v_mov_b32_e32 v166, 0
	v_mov_b32_e32 v167, 0
	v_exp_f32_e32 v4, v4
	v_exp_f32_e32 v5, v5
	v_exp_f32_e32 v8, v8
	v_exp_f32_e32 v9, v9
	v_exp_f32_e32 v12, v12
	v_exp_f32_e32 v13, v13
	v_exp_f32_e32 v16, v16
	v_exp_f32_e32 v17, v23
	v_cvt_pk_fp8_f32 v164, v2, v3
	v_cvt_pk_fp8_f32 v165, v6, v7
	v_cvt_pk_fp8_f32 v166, v10, v11
	v_cvt_pk_fp8_f32 v167, v14, v15
	s_lshl_b32 s0, s22, 11
	s_add_i32 s0, s0, 0
	s_add_i32 s0, s0, 0x18000
	v_cvt_pk_fp8_f32 v164, v4, v5 op_sel:[0,0,1]
	v_cvt_pk_fp8_f32 v165, v8, v9 op_sel:[0,0,1]
	v_cvt_pk_fp8_f32 v166, v12, v13 op_sel:[0,0,1]
	v_cvt_pk_fp8_f32 v167, v16, v17 op_sel:[0,0,1]
	v_lshl_add_u32 v193, v198, 5, s0
	v_lshrrev_b32_e32 v3, 2, v0
	v_lshlrev_b32_e32 v6, 1, v183
	s_lshl_b32 s0, s20, 20
	v_bfe_u32 v4, v0, 2, 2
	v_lshl_or_b32 v5, v1, 6, s24
	v_bitop3_b32 v3, v6, v3, 3 bitop3:0x78
	s_or_b32 s18, s0, s23
	v_lshl_add_u32 v194, s34, 4, v193
	v_lshl_or_b32 v195, v3, 4, v5
	v_bitop3_b32 v3, v6, v4, 1 bitop3:0x36
	v_add3_u32 v4, s21, v20, v21
	s_add_u32 s0, s6, s18
	ds_write_b128 v194, v[164:167]
	v_lshl_or_b32 v196, v3, 4, v5
	v_ashrrev_i32_e32 v5, 31, v4
	s_addc_u32 s1, s7, 0
	s_waitcnt vmcnt(2) lgkmcnt(0)
	s_barrier
	s_mov_b64 s[60:61], s[0:1]
	v_lshl_add_u64 v[170:171], s[0:1], 0, v[4:5]
	v_add3_u32 v4, s21, v18, v19
	s_add_u32 s0, s8, s18
	v_mov_b32_e32 v2, 0
	v_ashrrev_i32_e32 v5, 31, v4
	s_addc_u32 s1, s9, 0
	s_mov_b32 s39, 0
	s_mov_b32 s40, 1
	s_mov_b64 s[64:65], s[0:1]
	v_lshl_add_u64 v[172:173], s[0:1], 0, v[4:5]
	s_mov_b64 s[6:7], 0
	s_movk_i32 s41, 0x2000
	s_mov_b64 s[8:9], 0xc000
	s_mov_b64 s[18:19], 0xe000
	s_mov_b64 s[20:21], 0x8000
	s_mov_b64 s[22:23], 0xa000
	s_mov_b32 s42, 0x42966666
	v_mov_b32_e32 v82, 0x4b400000
	v_mov_b32_e32 v100, 0x38383838
	s_mov_b32 s0, 0
	s_mov_b32 s43, 1
	v_mov_b32_e32 v3, v2
	v_mov_b32_e32 v4, v2
	v_mov_b32_e32 v5, v2
	v_mov_b32_e32 v6, v2
	v_mov_b32_e32 v7, v2
	v_mov_b32_e32 v8, v2
	v_mov_b32_e32 v9, v2
	v_mov_b32_e32 v10, v2
	v_mov_b32_e32 v11, v2
	v_mov_b32_e32 v12, v2
	v_mov_b32_e32 v13, v2
	v_mov_b32_e32 v14, v2
	v_mov_b32_e32 v15, v2
	v_mov_b32_e32 v16, v2
	v_mov_b32_e32 v17, v2
	v_mov_b32_e32 v18, v2
	v_mov_b32_e32 v19, v2
	v_mov_b32_e32 v20, v2
	v_mov_b32_e32 v21, v2
	v_mov_b32_e32 v22, v2
	v_mov_b32_e32 v23, v2
	v_mov_b32_e32 v24, v2
	v_mov_b32_e32 v25, v2
	v_mov_b32_e32 v26, v2
	v_mov_b32_e32 v27, v2
	v_mov_b32_e32 v28, v2
	v_mov_b32_e32 v29, v2
	v_mov_b32_e32 v30, v2
	v_mov_b32_e32 v31, v2
	v_mov_b32_e32 v32, v2
	v_mov_b32_e32 v33, v2
	v_mov_b32_e32 v34, v2
	v_mov_b32_e32 v35, v2
	v_mov_b32_e32 v36, v2
	v_mov_b32_e32 v37, v2
	v_mov_b32_e32 v38, v2
	v_mov_b32_e32 v39, v2
	v_mov_b32_e32 v40, v2
	v_mov_b32_e32 v41, v2
	v_mov_b32_e32 v42, v2
	v_mov_b32_e32 v43, v2
	v_mov_b32_e32 v44, v2
	v_mov_b32_e32 v45, v2
	v_mov_b32_e32 v46, v2
	v_mov_b32_e32 v47, v2
	v_mov_b32_e32 v48, v2
	v_mov_b32_e32 v49, v2
	v_mov_b32_e32 v50, v2
	v_mov_b32_e32 v51, v2
	v_mov_b32_e32 v52, v2
	v_mov_b32_e32 v53, v2
	v_mov_b32_e32 v54, v2
	v_mov_b32_e32 v55, v2
	v_mov_b32_e32 v56, v2
	v_mov_b32_e32 v57, v2
	v_mov_b32_e32 v58, v2
	v_mov_b32_e32 v59, v2
	v_mov_b32_e32 v60, v2
	v_mov_b32_e32 v61, v2
	v_mov_b32_e32 v62, v2
	v_mov_b32_e32 v63, v2
	v_mov_b32_e32 v64, v2
	v_mov_b32_e32 v65, v2
	v_mov_b32_e32 v66, v2
	v_mov_b32_e32 v67, v2
	v_mov_b32_e32 v68, v2
	v_mov_b32_e32 v69, v2
	v_mov_b32_e32 v70, v2
	v_mov_b32_e32 v71, v2
	v_mov_b32_e32 v72, v2
	v_mov_b32_e32 v73, v2
	v_mov_b32_e32 v74, v2
	v_mov_b32_e32 v75, v2
	v_mov_b32_e32 v76, v2
	v_mov_b32_e32 v77, v2
	v_mov_b32_e32 v78, v2
	v_mov_b32_e32 v79, v2
	v_mov_b32_e32 v80, v2
	v_mov_b32_e32 v81, v2
	v_mov_b32_e32 v101, v100
	v_mov_b32_e32 v102, v100
	v_mov_b32_e32 v103, v100
	v_mov_b32_e32 v104, v100
	v_mov_b32_e32 v105, v100
	v_mov_b32_e32 v106, v100
	v_mov_b32_e32 v107, v100
	v_mov_b32_e32 v226, 0x4b400000
	v_mov_b32_e32 v227, v226
	v_mov_b32_e32 v228, v226
	v_mov_b32_e32 v229, v226
	v_mov_b32_e32 v230, v226
	v_mov_b32_e32 v231, v226
	v_mov_b32_e32 v232, v226
	v_mov_b32_e32 v233, v226
	v_mov_b32_e32 v234, v226
	v_mov_b32_e32 v235, v226
	v_mov_b32_e32 v236, v226
	v_mov_b32_e32 v237, v226
	v_mov_b32_e32 v238, v226
	v_mov_b32_e32 v239, v226
	v_mov_b32_e32 v240, v226
	v_mov_b32_e32 v241, v226
	v_add_u32_e32 v250, 0xc000, v184
	v_add_u32_e32 v185, v185, v250
	v_add_u32_e32 v186, v186, v250
	v_add_u32_e32 v187, v187, v250
	v_add_u32_e32 v188, v188, v250
	v_add_u32_e32 v189, v189, v250
	v_add_u32_e32 v190, v190, v250
	v_add_u32_e32 v191, v191, v250
	v_add_u32_e32 v192, v192, v250
	v_subrev_u32_e32 v252, s60, v170
	v_subrev_u32_e32 v255, s64, v172
	s_sub_u32 s1, s64, s60
	s_add_i32 s1, s1, 0xffffc000
	v_add_u32_e32 v254, 0x2000, v252
	v_add_u32_e32 v255, s1, v255
	v_add_u32_e32 v201, 0x2000, v255
	s_add_u32 s60, s60, 0xc000
	s_addc_u32 s61, s61, 0
	s_mov_b64 s[54:55], -1
	v_mfma_i32_32x32x32_i8 v[84:99], v[218:221], v[132:135], v[226:241]
	v_mfma_i32_32x32x32_i8 v[84:99], v[222:225], v[136:139], v[84:99]
.Lat_u0:
	ds_read_b128 v[108:111], v193
	ds_read_b128 v[112:115], v193 offset:16
	v_mfma_i32_32x32x32_i8 v[84:99], v[242:245], v[140:143], v[84:99]
	ds_read_b128 v[116:119], v195 offset:6144
	ds_read_b128 v[120:123], v196 offset:6144
	s_cmp_gt_u32 s43, 29
	s_cbranch_scc1 .Lat_nok0
	s_add_i32 m0, s31, 49152
	ds_read_b128 v[124:127], v195 offset:4096
	global_load_lds_dwordx4 v252, s[60:61]
	s_add_i32 m0, s31, 57344
	v_mfma_i32_32x32x32_i8 v[84:99], v[246:249], v[144:147], v[84:99]
	global_load_lds_dwordx4 v254, s[60:61]
	s_branch .Lat_k0
.Lat_nok0:
	ds_read_b128 v[124:127], v195 offset:4096
	v_mfma_i32_32x32x32_i8 v[84:99], v[246:249], v[144:147], v[84:99]
.Lat_k0:
	ds_read_b128 v[128:131], v196 offset:4096
	v_mfma_i32_32x32x32_i8 v[84:99], v[202:205], v[148:151], v[84:99]
	ds_read_b128 v[202:205], v195
	v_mfma_i32_32x32x32_i8 v[84:99], v[206:209], v[152:155], v[84:99]
	ds_read_b128 v[206:209], v196
	v_mfma_i32_32x32x32_i8 v[84:99], v[210:213], v[156:159], v[84:99]
	ds_read_b128 v[210:213], v195 offset:2048
	v_mfma_i32_32x32x32_i8 v[84:99], v[214:217], v[160:163], v[84:99]
	ds_read_b128 v[214:217], v196 offset:2048
	v_readlane_b32 s50, v182, s43
	s_waitcnt lgkmcnt(6)
	v_mfma_f32_32x32x64_f8f6f4 v[2:17], v[108:115], v[116:123], v[2:17]
	ds_read_b128 v[218:221], v185 offset:32768
	ds_read_b128 v[222:225], v186 offset:32768
	ds_read_b128 v[242:245], v187 offset:32768
	ds_read_b128 v[246:249], v188 offset:32768
	v_mul_f32_e32 v82, s50, v168
	v_mul_f32_e32 v250, 0x3db8aa3b, v82
	v_fmamk_f32 v251, v250, 0xcb400000, v200
	s_cmp_gt_u32 s43, 30
	s_cbranch_scc1 .Lat_nov0
	s_add_i32 m0, s31, 32768
	v_max_i32_e32 v83, v84, v85
	global_load_lds_dwordx4 v255, s[60:61]
	s_add_i32 m0, s31, 40960
	v_max3_i32 v83, v83, v86, v87
	global_load_lds_dwordx4 v201, s[60:61]
	s_branch .Lat_v0

.Lat_v0:
	v_max3_i32 v83, v83, v88, v89
	v_max3_i32 v83, v83, v90, v91
	v_max3_i32 v83, v83, v92, v93
	v_max3_i32 v83, v83, v94, v95
	v_max3_i32 v83, v83, v96, v97
	v_max3_i32 v83, v83, v98, v99
	s_waitcnt lgkmcnt(8)
	v_mfma_f32_32x32x64_f8f6f4 v[18:33], v[108:115], v[124:131], v[18:33]
	v_fma_f32 v84, v84, v250, v251
	v_fma_f32 v85, v85, v250, v251
	v_fma_f32 v86, v86, v250, v251
	v_fma_f32 v87, v87, v250, v251
	v_add_f32_e32 v83, 0xcb400000, v83
	v_exp_f32_e32 v84, v84
	v_exp_f32_e32 v85, v85
	v_fma_f32 v82, v82, v83, -v197
	v_exp_f32_e32 v86, v86
	v_exp_f32_e32 v87, v87
	v_fma_f32 v88, v88, v250, v251
	v_fma_f32 v89, v89, v250, v251
	v_fma_f32 v90, v90, v250, v251
	v_fma_f32 v91, v91, v250, v251
	v_cmp_ge_f32_e64 s[52:53], s42, v82
	v_mfma_f32_32x32x64_f8f6f4 v[66:81], v[108:115], v[100:107], v[66:81]
	v_cvt_pk_fp8_f32 v164, v84, v85
	v_cvt_pk_fp8_f32 v164, v86, v87 op_sel:[0,0,1]
	v_exp_f32_e32 v88, v88
	v_exp_f32_e32 v89, v89
	v_exp_f32_e32 v90, v90
	v_exp_f32_e32 v91, v91
	v_fma_f32 v92, v92, v250, v251
	v_fma_f32 v93, v93, v250, v251
	v_fma_f32 v94, v94, v250, v251
	v_fma_f32 v95, v95, v250, v251
	v_cvt_pk_fp8_f32 v165, v88, v89
	v_cvt_pk_fp8_f32 v165, v90, v91 op_sel:[0,0,1]
	v_exp_f32_e32 v92, v92
	v_exp_f32_e32 v93, v93
	v_exp_f32_e32 v94, v94
	v_exp_f32_e32 v95, v95
	s_waitcnt lgkmcnt(6)
	v_mfma_f32_32x32x64_f8f6f4 v[50:65], v[108:115], v[202:209], v[50:65]
	ds_read_b128 v[202:205], v189 offset:32768
	ds_read_b128 v[206:209], v190 offset:32768
	v_fma_f32 v96, v96, v250, v251
	v_fma_f32 v97, v97, v250, v251
	v_fma_f32 v98, v98, v250, v251
	v_fma_f32 v99, v99, v250, v251
	v_cvt_pk_fp8_f32 v166, v92, v93
	v_cvt_pk_fp8_f32 v166, v94, v95 op_sel:[0,0,1]
	v_exp_f32_e32 v96, v96
	v_exp_f32_e32 v97, v97
	v_exp_f32_e32 v98, v98
	v_exp_f32_e32 v99, v99
	s_and_b64 s[54:55], s[54:55], s[52:53]
	s_add_u32 s60, s60, 0x4000
	s_addc_u32 s61, s61, 0
	v_cvt_pk_fp8_f32 v167, v96, v97
	v_cvt_pk_fp8_f32 v167, v98, v99 op_sel:[0,0,1]
	ds_write_b128 v194, v[164:167] offset:8192
	s_waitcnt lgkmcnt(7)
	v_mfma_f32_32x32x64_f8f6f4 v[34:49], v[108:115], v[210:217], v[34:49]
	ds_read_b128 v[210:213], v191 offset:32768
	ds_read_b128 v[214:217], v192 offset:32768
	s_add_i32 s43, s43, 1
	s_cmp_eq_u32 s43, 32
	s_cbranch_scc1 .Lat_last
	s_waitcnt lgkmcnt(7)
	v_mfma_i32_32x32x32_i8 v[84:99], v[218:221], v[132:135], v[226:241]
	v_mfma_i32_32x32x32_i8 v[84:99], v[222:225], v[136:139], v[84:99]
	s_waitcnt vmcnt(2) lgkmcnt(0)
	s_barrier
.Lat_u1:
	ds_read_b128 v[108:111], v193 offset:8192
	ds_read_b128 v[112:115], v193 offset:8208
	v_mfma_i32_32x32x32_i8 v[84:99], v[242:245], v[140:143], v[84:99]
	ds_read_b128 v[116:119], v195 offset:22528
	ds_read_b128 v[120:123], v196 offset:22528
	s_add_i32 m0, s31, 65536
	ds_read_b128 v[124:127], v195 offset:20480
	global_load_lds_dwordx4 v252, s[60:61]
	s_add_i32 m0, s31, 73728
	v_mfma_i32_32x32x32_i8 v[84:99], v[246:249], v[144:147], v[84:99]
	global_load_lds_dwordx4 v254, s[60:61]
	ds_read_b128 v[128:131], v196 offset:20480
	v_mfma_i32_32x32x32_i8 v[84:99], v[202:205], v[148:151], v[84:99]
	ds_read_b128 v[202:205], v195 offset:16384
	v_mfma_i32_32x32x32_i8 v[84:99], v[206:209], v[152:155], v[84:99]
	ds_read_b128 v[206:209], v196 offset:16384
	v_mfma_i32_32x32x32_i8 v[84:99], v[210:213], v[156:159], v[84:99]
	ds_read_b128 v[210:213], v195 offset:18432
	v_mfma_i32_32x32x32_i8 v[84:99], v[214:217], v[160:163], v[84:99]
	ds_read_b128 v[214:217], v196 offset:18432
	v_readlane_b32 s50, v182, s43
	s_waitcnt lgkmcnt(6)
	v_mfma_f32_32x32x64_f8f6f4 v[2:17], v[108:115], v[116:123], v[2:17]
	ds_read_b128 v[218:221], v185
	ds_read_b128 v[222:225], v186
	ds_read_b128 v[242:245], v187
	ds_read_b128 v[246:249], v188
	v_mul_f32_e32 v82, s50, v168
	v_mul_f32_e32 v250, 0x3db8aa3b, v82
	v_fmamk_f32 v251, v250, 0xcb400000, v200
	s_mov_b32 m0, s31
	v_max_i32_e32 v83, v84, v85
	global_load_lds_dwordx4 v255, s[60:61]
	s_add_i32 m0, s31, 8192
	v_max3_i32 v83, v83, v86, v87
	global_load_lds_dwordx4 v201, s[60:61]
	v_max3_i32 v83, v83, v88, v89
	v_max3_i32 v83, v83, v90, v91
	v_max3_i32 v83, v83, v92, v93
	v_max3_i32 v83, v83, v94, v95
	v_max3_i32 v83, v83, v96, v97
	v_max3_i32 v83, v83, v98, v99
	s_waitcnt lgkmcnt(8)
	v_mfma_f32_32x32x64_f8f6f4 v[18:33], v[108:115], v[124:131], v[18:33]
	v_fma_f32 v84, v84, v250, v251
	v_fma_f32 v85, v85, v250, v251
	v_fma_f32 v86, v86, v250, v251
	v_fma_f32 v87, v87, v250, v251
	v_add_f32_e32 v83, 0xcb400000, v83
	v_exp_f32_e32 v84, v84
	v_exp_f32_e32 v85, v85
	v_fma_f32 v82, v82, v83, -v197
	v_exp_f32_e32 v86, v86
	v_exp_f32_e32 v87, v87
	v_fma_f32 v88, v88, v250, v251
	v_fma_f32 v89, v89, v250, v251
	v_fma_f32 v90, v90, v250, v251
	v_fma_f32 v91, v91, v250, v251
	v_cmp_ge_f32_e64 s[52:53], s42, v82
	v_mfma_f32_32x32x64_f8f6f4 v[66:81], v[108:115], v[100:107], v[66:81]
	v_cvt_pk_fp8_f32 v164, v84, v85
	v_cvt_pk_fp8_f32 v164, v86, v87 op_sel:[0,0,1]
	v_exp_f32_e32 v88, v88
	v_exp_f32_e32 v89, v89
	v_exp_f32_e32 v90, v90
	v_exp_f32_e32 v91, v91
	v_fma_f32 v92, v92, v250, v251
	v_fma_f32 v93, v93, v250, v251
	v_fma_f32 v94, v94, v250, v251
	v_fma_f32 v95, v95, v250, v251
	v_cvt_pk_fp8_f32 v165, v88, v89
	v_cvt_pk_fp8_f32 v165, v90, v91 op_sel:[0,0,1]
	v_exp_f32_e32 v92, v92
	v_exp_f32_e32 v93, v93
	v_exp_f32_e32 v94, v94
	v_exp_f32_e32 v95, v95
	s_waitcnt lgkmcnt(6)
	v_mfma_f32_32x32x64_f8f6f4 v[50:65], v[108:115], v[202:209], v[50:65]
	ds_read_b128 v[202:205], v189
	ds_read_b128 v[206:209], v190
	v_fma_f32 v96, v96, v250, v251
	v_fma_f32 v97, v97, v250, v251
	v_fma_f32 v98, v98, v250, v251
	v_fma_f32 v99, v99, v250, v251
	v_cvt_pk_fp8_f32 v166, v92, v93
	v_cvt_pk_fp8_f32 v166, v94, v95 op_sel:[0,0,1]
	v_exp_f32_e32 v96, v96
	v_exp_f32_e32 v97, v97
	v_exp_f32_e32 v98, v98
	v_exp_f32_e32 v99, v99
	s_and_b64 s[54:55], s[54:55], s[52:53]
	s_add_u32 s60, s60, 0x4000
	s_addc_u32 s61, s61, 0
	v_cvt_pk_fp8_f32 v167, v96, v97
	v_cvt_pk_fp8_f32 v167, v98, v99 op_sel:[0,0,1]
	ds_write_b128 v194, v[164:167]
	s_waitcnt lgkmcnt(7)
	v_mfma_f32_32x32x64_f8f6f4 v[34:49], v[108:115], v[210:217], v[34:49]
	ds_read_b128 v[210:213], v191
	ds_read_b128 v[214:217], v192
	s_add_i32 s43, s43, 1
	s_waitcnt lgkmcnt(7)
	v_mfma_i32_32x32x32_i8 v[84:99], v[218:221], v[132:135], v[226:241]
	v_mfma_i32_32x32x32_i8 v[84:99], v[222:225], v[136:139], v[84:99]
	s_waitcnt vmcnt(2) lgkmcnt(0)
	s_barrier
.Lat_u2:
	ds_read_b128 v[108:111], v193
	ds_read_b128 v[112:115], v193 offset:16
	v_mfma_i32_32x32x32_i8 v[84:99], v[242:245], v[140:143], v[84:99]
	ds_read_b128 v[116:119], v195 offset:38912
	ds_read_b128 v[120:123], v196 offset:38912
	s_add_i32 m0, s31, 81920
	ds_read_b128 v[124:127], v195 offset:36864
	global_load_lds_dwordx4 v252, s[60:61]
	s_add_i32 m0, s31, 90112
	v_mfma_i32_32x32x32_i8 v[84:99], v[246:249], v[144:147], v[84:99]
	global_load_lds_dwordx4 v254, s[60:61]
	ds_read_b128 v[128:131], v196 offset:36864
	v_mfma_i32_32x32x32_i8 v[84:99], v[202:205], v[148:151], v[84:99]
	ds_read_b128 v[202:205], v195 offset:32768
	v_mfma_i32_32x32x32_i8 v[84:99], v[206:209], v[152:155], v[84:99]
	ds_read_b128 v[206:209], v196 offset:32768
	v_mfma_i32_32x32x32_i8 v[84:99], v[210:213], v[156:159], v[84:99]
	ds_read_b128 v[210:213], v195 offset:34816
	v_mfma_i32_32x32x32_i8 v[84:99], v[214:217], v[160:163], v[84:99]
	ds_read_b128 v[214:217], v196 offset:34816
	v_readlane_b32 s50, v182, s43
	s_waitcnt lgkmcnt(6)
	v_mfma_f32_32x32x64_f8f6f4 v[2:17], v[108:115], v[116:123], v[2:17]
	ds_read_b128 v[218:221], v185 offset:16384
	ds_read_b128 v[222:225], v186 offset:16384
	ds_read_b128 v[242:245], v187 offset:16384
	ds_read_b128 v[246:249], v188 offset:16384
	v_mul_f32_e32 v82, s50, v168
	v_mul_f32_e32 v250, 0x3db8aa3b, v82
	v_fmamk_f32 v251, v250, 0xcb400000, v200
	s_add_i32 m0, s31, 16384
	v_max_i32_e32 v83, v84, v85
	global_load_lds_dwordx4 v255, s[60:61]
	s_add_i32 m0, s31, 24576
	v_max3_i32 v83, v83, v86, v87
	global_load_lds_dwordx4 v201, s[60:61]
	v_max3_i32 v83, v83, v88, v89
	v_max3_i32 v83, v83, v90, v91
	v_max3_i32 v83, v83, v92, v93
	v_max3_i32 v83, v83, v94, v95
	v_max3_i32 v83, v83, v96, v97
	v_max3_i32 v83, v83, v98, v99
	s_waitcnt lgkmcnt(8)
	v_mfma_f32_32x32x64_f8f6f4 v[18:33], v[108:115], v[124:131], v[18:33]
	v_fma_f32 v84, v84, v250, v251
	v_fma_f32 v85, v85, v250, v251
	v_fma_f32 v86, v86, v250, v251
	v_fma_f32 v87, v87, v250, v251
	v_add_f32_e32 v83, 0xcb400000, v83
	v_exp_f32_e32 v84, v84
	v_exp_f32_e32 v85, v85
	v_fma_f32 v82, v82, v83, -v197
	v_exp_f32_e32 v86, v86
	v_exp_f32_e32 v87, v87
	v_fma_f32 v88, v88, v250, v251
	v_fma_f32 v89, v89, v250, v251
	v_fma_f32 v90, v90, v250, v251
	v_fma_f32 v91, v91, v250, v251
	v_cmp_ge_f32_e64 s[52:53], s42, v82
	v_mfma_f32_32x32x64_f8f6f4 v[66:81], v[108:115], v[100:107], v[66:81]
	v_cvt_pk_fp8_f32 v164, v84, v85
	v_cvt_pk_fp8_f32 v164, v86, v87 op_sel:[0,0,1]
	v_exp_f32_e32 v88, v88
	v_exp_f32_e32 v89, v89
	v_exp_f32_e32 v90, v90
	v_exp_f32_e32 v91, v91
	v_fma_f32 v92, v92, v250, v251
	v_fma_f32 v93, v93, v250, v251
	v_fma_f32 v94, v94, v250, v251
	v_fma_f32 v95, v95, v250, v251
	v_cvt_pk_fp8_f32 v165, v88, v89
	v_cvt_pk_fp8_f32 v165, v90, v91 op_sel:[0,0,1]
	v_exp_f32_e32 v92, v92
	v_exp_f32_e32 v93, v93
	v_exp_f32_e32 v94, v94
	v_exp_f32_e32 v95, v95
	s_waitcnt lgkmcnt(6)
	v_mfma_f32_32x32x64_f8f6f4 v[50:65], v[108:115], v[202:209], v[50:65]
	ds_read_b128 v[202:205], v189 offset:16384
	ds_read_b128 v[206:209], v190 offset:16384
	v_fma_f32 v96, v96, v250, v251
	v_fma_f32 v97, v97, v250, v251
	v_fma_f32 v98, v98, v250, v251
	v_fma_f32 v99, v99, v250, v251
	v_cvt_pk_fp8_f32 v166, v92, v93
	v_cvt_pk_fp8_f32 v166, v94, v95 op_sel:[0,0,1]
	v_exp_f32_e32 v96, v96
	v_exp_f32_e32 v97, v97
	v_exp_f32_e32 v98, v98
	v_exp_f32_e32 v99, v99
	s_and_b64 s[54:55], s[54:55], s[52:53]
	s_add_u32 s60, s60, 0x4000
	s_addc_u32 s61, s61, 0
	v_cvt_pk_fp8_f32 v167, v96, v97
	v_cvt_pk_fp8_f32 v167, v98, v99 op_sel:[0,0,1]
	ds_write_b128 v194, v[164:167] offset:8192
	s_waitcnt lgkmcnt(7)
	v_mfma_f32_32x32x64_f8f6f4 v[34:49], v[108:115], v[210:217], v[34:49]
	ds_read_b128 v[210:213], v191 offset:16384
	ds_read_b128 v[214:217], v192 offset:16384
	s_add_i32 s43, s43, 1
	s_waitcnt lgkmcnt(7)
	v_mfma_i32_32x32x32_i8 v[84:99], v[218:221], v[132:135], v[226:241]
	v_mfma_i32_32x32x32_i8 v[84:99], v[222:225], v[136:139], v[84:99]
	s_waitcnt vmcnt(2) lgkmcnt(0)
	s_barrier
.Lat_u3:
	ds_read_b128 v[108:111], v193 offset:8192
	ds_read_b128 v[112:115], v193 offset:8208
	v_mfma_i32_32x32x32_i8 v[84:99], v[242:245], v[140:143], v[84:99]
	ds_read_b128 v[116:119], v195 offset:6144
	ds_read_b128 v[120:123], v196 offset:6144
	s_add_i32 m0, s31, 49152
	ds_read_b128 v[124:127], v195 offset:4096
	global_load_lds_dwordx4 v252, s[60:61]
	s_add_i32 m0, s31, 57344
	v_mfma_i32_32x32x32_i8 v[84:99], v[246:249], v[144:147], v[84:99]
	global_load_lds_dwordx4 v254, s[60:61]
	ds_read_b128 v[128:131], v196 offset:4096
	v_mfma_i32_32x32x32_i8 v[84:99], v[202:205], v[148:151], v[84:99]
	ds_read_b128 v[202:205], v195
	v_mfma_i32_32x32x32_i8 v[84:99], v[206:209], v[152:155], v[84:99]
	ds_read_b128 v[206:209], v196
	v_mfma_i32_32x32x32_i8 v[84:99], v[210:213], v[156:159], v[84:99]
	ds_read_b128 v[210:213], v195 offset:2048
	v_mfma_i32_32x32x32_i8 v[84:99], v[214:217], v[160:163], v[84:99]
	ds_read_b128 v[214:217], v196 offset:2048
	v_readlane_b32 s50, v182, s43
	s_waitcnt lgkmcnt(6)
	v_mfma_f32_32x32x64_f8f6f4 v[2:17], v[108:115], v[116:123], v[2:17]
	ds_read_b128 v[218:221], v185 offset:32768
	ds_read_b128 v[222:225], v186 offset:32768
	ds_read_b128 v[242:245], v187 offset:32768
	ds_read_b128 v[246:249], v188 offset:32768
	v_mul_f32_e32 v82, s50, v168
	v_mul_f32_e32 v250, 0x3db8aa3b, v82
	v_fmamk_f32 v251, v250, 0xcb400000, v200
	s_add_i32 m0, s31, 32768
	v_max_i32_e32 v83, v84, v85
	global_load_lds_dwordx4 v255, s[60:61]
	s_add_i32 m0, s31, 40960
	v_max3_i32 v83, v83, v86, v87
	global_load_lds_dwordx4 v201, s[60:61]
	v_max3_i32 v83, v83, v88, v89
	v_max3_i32 v83, v83, v90, v91
	v_max3_i32 v83, v83, v92, v93
	v_max3_i32 v83, v83, v94, v95
	v_max3_i32 v83, v83, v96, v97
	v_max3_i32 v83, v83, v98, v99
	s_waitcnt lgkmcnt(8)
	v_mfma_f32_32x32x64_f8f6f4 v[18:33], v[108:115], v[124:131], v[18:33]
	v_fma_f32 v84, v84, v250, v251
	v_fma_f32 v85, v85, v250, v251
	v_fma_f32 v86, v86, v250, v251
	v_fma_f32 v87, v87, v250, v251
	v_add_f32_e32 v83, 0xcb400000, v83
	v_exp_f32_e32 v84, v84
	v_exp_f32_e32 v85, v85
	v_fma_f32 v82, v82, v83, -v197
	v_exp_f32_e32 v86, v86
	v_exp_f32_e32 v87, v87
	v_fma_f32 v88, v88, v250, v251
	v_fma_f32 v89, v89, v250, v251
	v_fma_f32 v90, v90, v250, v251
	v_fma_f32 v91, v91, v250, v251
	v_cmp_ge_f32_e64 s[52:53], s42, v82
	v_mfma_f32_32x32x64_f8f6f4 v[66:81], v[108:115], v[100:107], v[66:81]
	v_cvt_pk_fp8_f32 v164, v84, v85
	v_cvt_pk_fp8_f32 v164, v86, v87 op_sel:[0,0,1]
	v_exp_f32_e32 v88, v88
	v_exp_f32_e32 v89, v89
	v_exp_f32_e32 v90, v90
	v_exp_f32_e32 v91, v91
	v_fma_f32 v92, v92, v250, v251
	v_fma_f32 v93, v93, v250, v251
	v_fma_f32 v94, v94, v250, v251
	v_fma_f32 v95, v95, v250, v251
	v_cvt_pk_fp8_f32 v165, v88, v89
	v_cvt_pk_fp8_f32 v165, v90, v91 op_sel:[0,0,1]
	v_exp_f32_e32 v92, v92
	v_exp_f32_e32 v93, v93
	v_exp_f32_e32 v94, v94
	v_exp_f32_e32 v95, v95
	s_waitcnt lgkmcnt(6)
	v_mfma_f32_32x32x64_f8f6f4 v[50:65], v[108:115], v[202:209], v[50:65]
	ds_read_b128 v[202:205], v189 offset:32768
	ds_read_b128 v[206:209], v190 offset:32768
	v_fma_f32 v96, v96, v250, v251
	v_fma_f32 v97, v97, v250, v251
	v_fma_f32 v98, v98, v250, v251
	v_fma_f32 v99, v99, v250, v251
	v_cvt_pk_fp8_f32 v166, v92, v93
	v_cvt_pk_fp8_f32 v166, v94, v95 op_sel:[0,0,1]
	v_exp_f32_e32 v96, v96
	v_exp_f32_e32 v97, v97
	v_exp_f32_e32 v98, v98
	v_exp_f32_e32 v99, v99
	s_and_b64 s[54:55], s[54:55], s[52:53]
	s_add_u32 s60, s60, 0x4000
	s_addc_u32 s61, s61, 0
	v_cvt_pk_fp8_f32 v167, v96, v97
	v_cvt_pk_fp8_f32 v167, v98, v99 op_sel:[0,0,1]
	ds_write_b128 v194, v[164:167]
	s_waitcnt lgkmcnt(7)
	v_mfma_f32_32x32x64_f8f6f4 v[34:49], v[108:115], v[210:217], v[34:49]
	ds_read_b128 v[210:213], v191 offset:32768
	ds_read_b128 v[214:217], v192 offset:32768
	s_add_i32 s43, s43, 1
	s_waitcnt lgkmcnt(7)
	v_mfma_i32_32x32x32_i8 v[84:99], v[218:221], v[132:135], v[226:241]
	v_mfma_i32_32x32x32_i8 v[84:99], v[222:225], v[136:139], v[84:99]
	s_waitcnt vmcnt(2) lgkmcnt(0)
	s_barrier
.Lat_u4:
	ds_read_b128 v[108:111], v193
	ds_read_b128 v[112:115], v193 offset:16
	v_mfma_i32_32x32x32_i8 v[84:99], v[242:245], v[140:143], v[84:99]
	ds_read_b128 v[116:119], v195 offset:22528
	ds_read_b128 v[120:123], v196 offset:22528
	s_add_i32 m0, s31, 65536
	ds_read_b128 v[124:127], v195 offset:20480
	global_load_lds_dwordx4 v252, s[60:61]
	s_add_i32 m0, s31, 73728
	v_mfma_i32_32x32x32_i8 v[84:99], v[246:249], v[144:147], v[84:99]
	global_load_lds_dwordx4 v254, s[60:61]
	ds_read_b128 v[128:131], v196 offset:20480
	v_mfma_i32_32x32x32_i8 v[84:99], v[202:205], v[148:151], v[84:99]
	ds_read_b128 v[202:205], v195 offset:16384
	v_mfma_i32_32x32x32_i8 v[84:99], v[206:209], v[152:155], v[84:99]
	ds_read_b128 v[206:209], v196 offset:16384
	v_mfma_i32_32x32x32_i8 v[84:99], v[210:213], v[156:159], v[84:99]
	ds_read_b128 v[210:213], v195 offset:18432
	v_mfma_i32_32x32x32_i8 v[84:99], v[214:217], v[160:163], v[84:99]
	ds_read_b128 v[214:217], v196 offset:18432
	v_readlane_b32 s50, v182, s43
	s_waitcnt lgkmcnt(6)
	v_mfma_f32_32x32x64_f8f6f4 v[2:17], v[108:115], v[116:123], v[2:17]
	ds_read_b128 v[218:221], v185
	ds_read_b128 v[222:225], v186
	ds_read_b128 v[242:245], v187
	ds_read_b128 v[246:249], v188
	v_mul_f32_e32 v82, s50, v168
	v_mul_f32_e32 v250, 0x3db8aa3b, v82
	v_fmamk_f32 v251, v250, 0xcb400000, v200
	s_mov_b32 m0, s31
	v_max_i32_e32 v83, v84, v85
	global_load_lds_dwordx4 v255, s[60:61]
	s_add_i32 m0, s31, 8192
	v_max3_i32 v83, v83, v86, v87
	global_load_lds_dwordx4 v201, s[60:61]
	v_max3_i32 v83, v83, v88, v89
	v_max3_i32 v83, v83, v90, v91
	v_max3_i32 v83, v83, v92, v93
	v_max3_i32 v83, v83, v94, v95
	v_max3_i32 v83, v83, v96, v97
	v_max3_i32 v83, v83, v98, v99
	s_waitcnt lgkmcnt(8)
	v_mfma_f32_32x32x64_f8f6f4 v[18:33], v[108:115], v[124:131], v[18:33]
	v_fma_f32 v84, v84, v250, v251
	v_fma_f32 v85, v85, v250, v251
	v_fma_f32 v86, v86, v250, v251
	v_fma_f32 v87, v87, v250, v251
	v_add_f32_e32 v83, 0xcb400000, v83
	v_exp_f32_e32 v84, v84
	v_exp_f32_e32 v85, v85
	v_fma_f32 v82, v82, v83, -v197
	v_exp_f32_e32 v86, v86
	v_exp_f32_e32 v87, v87
	v_fma_f32 v88, v88, v250, v251
	v_fma_f32 v89, v89, v250, v251
	v_fma_f32 v90, v90, v250, v251
	v_fma_f32 v91, v91, v250, v251
	v_cmp_ge_f32_e64 s[52:53], s42, v82
	v_mfma_f32_32x32x64_f8f6f4 v[66:81], v[108:115], v[100:107], v[66:81]
	v_cvt_pk_fp8_f32 v164, v84, v85
	v_cvt_pk_fp8_f32 v164, v86, v87 op_sel:[0,0,1]
	v_exp_f32_e32 v88, v88
	v_exp_f32_e32 v89, v89
	v_exp_f32_e32 v90, v90
	v_exp_f32_e32 v91, v91
	v_fma_f32 v92, v92, v250, v251
	v_fma_f32 v93, v93, v250, v251
	v_fma_f32 v94, v94, v250, v251
	v_fma_f32 v95, v95, v250, v251
	v_cvt_pk_fp8_f32 v165, v88, v89
	v_cvt_pk_fp8_f32 v165, v90, v91 op_sel:[0,0,1]
	v_exp_f32_e32 v92, v92
	v_exp_f32_e32 v93, v93
	v_exp_f32_e32 v94, v94
	v_exp_f32_e32 v95, v95
	s_waitcnt lgkmcnt(6)
	v_mfma_f32_32x32x64_f8f6f4 v[50:65], v[108:115], v[202:209], v[50:65]
	ds_read_b128 v[202:205], v189
	ds_read_b128 v[206:209], v190
	v_fma_f32 v96, v96, v250, v251
	v_fma_f32 v97, v97, v250, v251
	v_fma_f32 v98, v98, v250, v251
	v_fma_f32 v99, v99, v250, v251
	v_cvt_pk_fp8_f32 v166, v92, v93
	v_cvt_pk_fp8_f32 v166, v94, v95 op_sel:[0,0,1]
	v_exp_f32_e32 v96, v96
	v_exp_f32_e32 v97, v97
	v_exp_f32_e32 v98, v98
	v_exp_f32_e32 v99, v99
	s_and_b64 s[54:55], s[54:55], s[52:53]
	s_add_u32 s60, s60, 0x4000
	s_addc_u32 s61, s61, 0
	v_cvt_pk_fp8_f32 v167, v96, v97
	v_cvt_pk_fp8_f32 v167, v98, v99 op_sel:[0,0,1]
	ds_write_b128 v194, v[164:167] offset:8192
	s_waitcnt lgkmcnt(7)
	v_mfma_f32_32x32x64_f8f6f4 v[34:49], v[108:115], v[210:217], v[34:49]
	ds_read_b128 v[210:213], v191
	ds_read_b128 v[214:217], v192
	s_add_i32 s43, s43, 1
	s_waitcnt lgkmcnt(7)
	v_mfma_i32_32x32x32_i8 v[84:99], v[218:221], v[132:135], v[226:241]
	v_mfma_i32_32x32x32_i8 v[84:99], v[222:225], v[136:139], v[84:99]
	s_waitcnt vmcnt(2) lgkmcnt(0)
	s_barrier
.Lat_u5:
	ds_read_b128 v[108:111], v193 offset:8192
	ds_read_b128 v[112:115], v193 offset:8208
	v_mfma_i32_32x32x32_i8 v[84:99], v[242:245], v[140:143], v[84:99]
	ds_read_b128 v[116:119], v195 offset:38912
	ds_read_b128 v[120:123], v196 offset:38912
	s_cmp_gt_u32 s43, 29
	s_cbranch_scc1 .Lat_nok5
	s_add_i32 m0, s31, 81920
	ds_read_b128 v[124:127], v195 offset:36864
	global_load_lds_dwordx4 v252, s[60:61]
	s_add_i32 m0, s31, 90112
	v_mfma_i32_32x32x32_i8 v[84:99], v[246:249], v[144:147], v[84:99]
	global_load_lds_dwordx4 v254, s[60:61]
	s_branch .Lat_k5
.Lat_nok5:
	ds_read_b128 v[124:127], v195 offset:36864
	v_mfma_i32_32x32x32_i8 v[84:99], v[246:249], v[144:147], v[84:99]
.Lat_k5:
	ds_read_b128 v[128:131], v196 offset:36864
	v_mfma_i32_32x32x32_i8 v[84:99], v[202:205], v[148:151], v[84:99]
	ds_read_b128 v[202:205], v195 offset:32768
	v_mfma_i32_32x32x32_i8 v[84:99], v[206:209], v[152:155], v[84:99]
	ds_read_b128 v[206:209], v196 offset:32768
	v_mfma_i32_32x32x32_i8 v[84:99], v[210:213], v[156:159], v[84:99]
	ds_read_b128 v[210:213], v195 offset:34816
	v_mfma_i32_32x32x32_i8 v[84:99], v[214:217], v[160:163], v[84:99]
	ds_read_b128 v[214:217], v196 offset:34816
	v_readlane_b32 s50, v182, s43
	s_waitcnt lgkmcnt(6)
	v_mfma_f32_32x32x64_f8f6f4 v[2:17], v[108:115], v[116:123], v[2:17]
	ds_read_b128 v[218:221], v185 offset:16384
	ds_read_b128 v[222:225], v186 offset:16384
	ds_read_b128 v[242:245], v187 offset:16384
	ds_read_b128 v[246:249], v188 offset:16384
	v_mul_f32_e32 v82, s50, v168
	v_mul_f32_e32 v250, 0x3db8aa3b, v82
	v_fmamk_f32 v251, v250, 0xcb400000, v200
	s_add_i32 m0, s31, 16384
	v_max_i32_e32 v83, v84, v85
	global_load_lds_dwordx4 v255, s[60:61]
	s_add_i32 m0, s31, 24576
	v_max3_i32 v83, v83, v86, v87
	global_load_lds_dwordx4 v201, s[60:61]
	v_max3_i32 v83, v83, v88, v89
	v_max3_i32 v83, v83, v90, v91
	v_max3_i32 v83, v83, v92, v93
	v_max3_i32 v83, v83, v94, v95
	v_max3_i32 v83, v83, v96, v97
	v_max3_i32 v83, v83, v98, v99
	s_waitcnt lgkmcnt(8)
	v_mfma_f32_32x32x64_f8f6f4 v[18:33], v[108:115], v[124:131], v[18:33]
	v_fma_f32 v84, v84, v250, v251
	v_fma_f32 v85, v85, v250, v251
	v_fma_f32 v86, v86, v250, v251
	v_fma_f32 v87, v87, v250, v251
	v_add_f32_e32 v83, 0xcb400000, v83
	v_exp_f32_e32 v84, v84
	v_exp_f32_e32 v85, v85
	v_fma_f32 v82, v82, v83, -v197
	v_exp_f32_e32 v86, v86
	v_exp_f32_e32 v87, v87
	v_fma_f32 v88, v88, v250, v251
	v_fma_f32 v89, v89, v250, v251
	v_fma_f32 v90, v90, v250, v251
	v_fma_f32 v91, v91, v250, v251
	v_cmp_ge_f32_e64 s[52:53], s42, v82
	v_mfma_f32_32x32x64_f8f6f4 v[66:81], v[108:115], v[100:107], v[66:81]
	v_cvt_pk_fp8_f32 v164, v84, v85
	v_cvt_pk_fp8_f32 v164, v86, v87 op_sel:[0,0,1]
	v_exp_f32_e32 v88, v88
	v_exp_f32_e32 v89, v89
	v_exp_f32_e32 v90, v90
	v_exp_f32_e32 v91, v91
	v_fma_f32 v92, v92, v250, v251
	v_fma_f32 v93, v93, v250, v251
	v_fma_f32 v94, v94, v250, v251
	v_fma_f32 v95, v95, v250, v251
	v_cvt_pk_fp8_f32 v165, v88, v89
	v_cvt_pk_fp8_f32 v165, v90, v91 op_sel:[0,0,1]
	v_exp_f32_e32 v92, v92
	v_exp_f32_e32 v93, v93
	v_exp_f32_e32 v94, v94
	v_exp_f32_e32 v95, v95
	s_waitcnt lgkmcnt(6)
	v_mfma_f32_32x32x64_f8f6f4 v[50:65], v[108:115], v[202:209], v[50:65]
	ds_read_b128 v[202:205], v189 offset:16384
	ds_read_b128 v[206:209], v190 offset:16384
	v_fma_f32 v96, v96, v250, v251
	v_fma_f32 v97, v97, v250, v251
	v_fma_f32 v98, v98, v250, v251
	v_fma_f32 v99, v99, v250, v251
	v_cvt_pk_fp8_f32 v166, v92, v93
	v_cvt_pk_fp8_f32 v166, v94, v95 op_sel:[0,0,1]
	v_exp_f32_e32 v96, v96
	v_exp_f32_e32 v97, v97
	v_exp_f32_e32 v98, v98
	v_exp_f32_e32 v99, v99
	s_and_b64 s[54:55], s[54:55], s[52:53]
	s_add_u32 s60, s60, 0x4000
	s_addc_u32 s61, s61, 0
	v_cvt_pk_fp8_f32 v167, v96, v97
	v_cvt_pk_fp8_f32 v167, v98, v99 op_sel:[0,0,1]
	ds_write_b128 v194, v[164:167]
	s_waitcnt lgkmcnt(7)
	v_mfma_f32_32x32x64_f8f6f4 v[34:49], v[108:115], v[210:217], v[34:49]
	ds_read_b128 v[210:213], v191 offset:16384
	ds_read_b128 v[214:217], v192 offset:16384
	s_add_i32 s43, s43, 1
	s_waitcnt lgkmcnt(7)
	v_mfma_i32_32x32x32_i8 v[84:99], v[218:221], v[132:135], v[226:241]
	v_mfma_i32_32x32x32_i8 v[84:99], v[222:225], v[136:139], v[84:99]
	s_cmp_gt_u32 s43, 30
	s_cbranch_scc1 .Lat_drain
	s_waitcnt vmcnt(2) lgkmcnt(0)
	s_barrier
	s_branch .Lat_u0

.Lat_last:
	s_waitcnt vmcnt(0) lgkmcnt(0)
	s_barrier
	s_cmp_lg_u64 s[54:55], exec
	s_cselect_b32 s1, 1, 0
	s_or_b32 s39, s39, s1
	v_add_u32_e32 v250, 0xc000, v184
	v_sub_u32_e32 v185, v185, v250
	v_sub_u32_e32 v186, v186, v250
	v_sub_u32_e32 v187, v187, v250
	v_sub_u32_e32 v188, v188, v250
	v_sub_u32_e32 v189, v189, v250
	v_sub_u32_e32 v190, v190, v250
	v_sub_u32_e32 v191, v191, v250
	v_sub_u32_e32 v192, v192, v250

.LBB2_31:
	s_or_b64 exec, exec, s[0:1]
	s_nop 1
	v_rcp_f32_e32 v66, v66
	s_and_b32 s0, s28, 0xffffff00
	s_lshl_b32 s1, s33, 9
	v_lshlrev_b32_e32 v1, 1, v1
	s_add_i32 s0, s0, 0
	v_lshl_or_b32 v82, v183, 11, s1
	v_mul_f32_e32 v18, v66, v18
	v_add3_u32 v1, s0, v1, v82
	v_cvt_pk_bf16_f32 v18, v18, s0
	ds_write_b16 v1, v18 offset:128
	v_rcp_f32_e32 v18, v67
	v_mul_f32_e32 v2, v66, v2
	v_cvt_pk_bf16_f32 v2, v2, s0
	ds_write_b16 v1, v2 offset:192
	v_mul_f32_e32 v2, v18, v51
	v_cvt_pk_bf16_f32 v2, v2, s0
	ds_write_b16 v1, v2 offset:512
	v_mul_f32_e32 v2, v18, v35
	v_cvt_pk_bf16_f32 v2, v2, s0
	ds_write_b16 v1, v2 offset:576
	v_mul_f32_e32 v2, v18, v19
	v_cvt_pk_bf16_f32 v2, v2, s0
	ds_write_b16 v1, v2 offset:640
	v_rcp_f32_e32 v2, v68
	v_mul_f32_e32 v3, v18, v3
	v_cvt_pk_bf16_f32 v3, v3, s0
	ds_write_b16 v1, v3 offset:704
	v_mul_f32_e32 v3, v2, v52
	v_cvt_pk_bf16_f32 v3, v3, s0
	ds_write_b16 v1, v3 offset:1024
	v_mul_f32_e32 v3, v2, v36
	v_cvt_pk_bf16_f32 v3, v3, s0
	ds_write_b16 v1, v3 offset:1088
	v_mul_f32_e32 v3, v2, v20
	v_cvt_pk_bf16_f32 v3, v3, s0
	ds_write_b16 v1, v3 offset:1152
	v_rcp_f32_e32 v3, v69
	v_mul_f32_e32 v2, v2, v4
	v_cvt_pk_bf16_f32 v2, v2, s0
	ds_write_b16 v1, v2 offset:1216
	v_mul_f32_e32 v2, v3, v53
	v_cvt_pk_bf16_f32 v2, v2, s0
	ds_write_b16 v1, v2 offset:1536
	v_mul_f32_e32 v2, v3, v37
	v_cvt_pk_bf16_f32 v2, v2, s0
	ds_write_b16 v1, v2 offset:1600
	v_mul_f32_e32 v2, v3, v21
	v_cvt_pk_bf16_f32 v2, v2, s0
	ds_write_b16 v1, v2 offset:1664
	v_rcp_f32_e32 v2, v70
	v_mul_f32_e32 v3, v3, v5
	v_cvt_pk_bf16_f32 v3, v3, s0
	ds_write_b16 v1, v3 offset:1728
	v_mul_f32_e32 v3, v2, v54
	v_cvt_pk_bf16_f32 v3, v3, s0
	ds_write_b16 v1, v3 offset:4096
	v_mul_f32_e32 v3, v2, v38
	v_cvt_pk_bf16_f32 v3, v3, s0
	ds_write_b16 v1, v3 offset:4160
	v_mul_f32_e32 v3, v2, v22
	v_cvt_pk_bf16_f32 v3, v3, s0
	ds_write_b16 v1, v3 offset:4224
	v_rcp_f32_e32 v3, v71
	v_mul_f32_e32 v2, v2, v6
	v_cvt_pk_bf16_f32 v2, v2, s0
	ds_write_b16 v1, v2 offset:4288
	v_mul_f32_e32 v2, v3, v55
	v_cvt_pk_bf16_f32 v2, v2, s0
	ds_write_b16 v1, v2 offset:4608
	v_mul_f32_e32 v2, v3, v39
	v_cvt_pk_bf16_f32 v2, v2, s0
	ds_write_b16 v1, v2 offset:4672
	v_mul_f32_e32 v2, v3, v23
	v_cvt_pk_bf16_f32 v2, v2, s0
	ds_write_b16 v1, v2 offset:4736
	v_rcp_f32_e32 v2, v72
	v_mul_f32_e32 v3, v3, v7
	v_cvt_pk_bf16_f32 v3, v3, s0
	ds_write_b16 v1, v3 offset:4800
	v_mul_f32_e32 v3, v2, v56
	v_cvt_pk_bf16_f32 v3, v3, s0
	ds_write_b16 v1, v3 offset:5120
	v_mul_f32_e32 v3, v2, v40
	v_cvt_pk_bf16_f32 v3, v3, s0
	ds_write_b16 v1, v3 offset:5184
	v_mul_f32_e32 v3, v2, v24
	v_cvt_pk_bf16_f32 v3, v3, s0
	ds_write_b16 v1, v3 offset:5248
	v_rcp_f32_e32 v3, v73
	v_mul_f32_e32 v2, v2, v8
	v_cvt_pk_bf16_f32 v2, v2, s0
	ds_write_b16 v1, v2 offset:5312
	v_mul_f32_e32 v2, v3, v57
	v_cvt_pk_bf16_f32 v2, v2, s0
	ds_write_b16 v1, v2 offset:5632
	v_mul_f32_e32 v2, v3, v41
	v_cvt_pk_bf16_f32 v2, v2, s0
	ds_write_b16 v1, v2 offset:5696
	v_mul_f32_e32 v2, v3, v25
	v_cvt_pk_bf16_f32 v2, v2, s0
	ds_write_b16 v1, v2 offset:5760
	v_rcp_f32_e32 v2, v74
	v_mul_f32_e32 v3, v3, v9
	v_cvt_pk_bf16_f32 v3, v3, s0
	ds_write_b16 v1, v3 offset:5824
	v_mul_f32_e32 v3, v2, v58
	v_cvt_pk_bf16_f32 v3, v3, s0
	ds_write_b16 v1, v3 offset:8192
	v_mul_f32_e32 v3, v2, v42
	v_cvt_pk_bf16_f32 v3, v3, s0
	ds_write_b16 v1, v3 offset:8256
	v_mul_f32_e32 v3, v2, v26
	v_cvt_pk_bf16_f32 v3, v3, s0
	ds_write_b16 v1, v3 offset:8320
	v_rcp_f32_e32 v3, v75
	v_mul_f32_e32 v2, v2, v10
	v_cvt_pk_bf16_f32 v2, v2, s0
	ds_write_b16 v1, v2 offset:8384
	v_mul_f32_e32 v2, v3, v59
	v_cvt_pk_bf16_f32 v2, v2, s0
	ds_write_b16 v1, v2 offset:8704
	v_mul_f32_e32 v2, v3, v43
	v_cvt_pk_bf16_f32 v2, v2, s0
	ds_write_b16 v1, v2 offset:8768
	v_mul_f32_e32 v2, v3, v27
	v_cvt_pk_bf16_f32 v2, v2, s0
	ds_write_b16 v1, v2 offset:8832
	v_rcp_f32_e32 v2, v76
	v_mul_f32_e32 v3, v3, v11
	v_cvt_pk_bf16_f32 v3, v3, s0
	ds_write_b16 v1, v3 offset:8896
	v_mul_f32_e32 v3, v2, v60
	v_cvt_pk_bf16_f32 v3, v3, s0
	ds_write_b16 v1, v3 offset:9216
	v_mul_f32_e32 v3, v2, v44
	v_cvt_pk_bf16_f32 v3, v3, s0
	ds_write_b16 v1, v3 offset:9280
	v_mul_f32_e32 v3, v2, v28
	v_cvt_pk_bf16_f32 v3, v3, s0
	ds_write_b16 v1, v3 offset:9344
	v_rcp_f32_e32 v3, v77
	v_mul_f32_e32 v2, v2, v12
	v_cvt_pk_bf16_f32 v2, v2, s0
	ds_write_b16 v1, v2 offset:9408
	v_mul_f32_e32 v2, v3, v61
	v_cvt_pk_bf16_f32 v2, v2, s0
	ds_write_b16 v1, v2 offset:9728
	v_mul_f32_e32 v2, v3, v45
	v_cvt_pk_bf16_f32 v2, v2, s0
	ds_write_b16 v1, v2 offset:9792
	v_mul_f32_e32 v2, v3, v29
	v_cvt_pk_bf16_f32 v2, v2, s0
	ds_write_b16 v1, v2 offset:9856
	v_rcp_f32_e32 v2, v78
	v_mul_f32_e32 v3, v3, v13
	v_cvt_pk_bf16_f32 v3, v3, s0
	ds_write_b16 v1, v3 offset:9920
	v_mul_f32_e32 v3, v2, v62
	v_cvt_pk_bf16_f32 v3, v3, s0
	ds_write_b16 v1, v3 offset:12288
	v_mul_f32_e32 v3, v2, v46
	v_cvt_pk_bf16_f32 v3, v3, s0
	ds_write_b16 v1, v3 offset:12352
	v_mul_f32_e32 v3, v2, v30
	v_cvt_pk_bf16_f32 v3, v3, s0
	ds_write_b16 v1, v3 offset:12416
	v_rcp_f32_e32 v3, v79
	v_mul_f32_e32 v2, v2, v14
	v_cvt_pk_bf16_f32 v2, v2, s0
	ds_write_b16 v1, v2 offset:12480
	v_mul_f32_e32 v2, v3, v63
	v_cvt_pk_bf16_f32 v2, v2, s0
	ds_write_b16 v1, v2 offset:12800
	v_mul_f32_e32 v2, v3, v47
	v_cvt_pk_bf16_f32 v2, v2, s0
	ds_write_b16 v1, v2 offset:12864
	v_mul_f32_e32 v2, v3, v31
	v_cvt_pk_bf16_f32 v2, v2, s0
	ds_write_b16 v1, v2 offset:12928
	v_rcp_f32_e32 v2, v80
	v_mul_f32_e32 v3, v3, v15
	v_cvt_pk_bf16_f32 v3, v3, s0
	ds_write_b16 v1, v3 offset:12992
	v_mul_f32_e32 v3, v2, v64
	v_cvt_pk_bf16_f32 v3, v3, s0
	ds_write_b16 v1, v3 offset:13312
	v_mul_f32_e32 v3, v2, v48
	v_cvt_pk_bf16_f32 v3, v3, s0
	ds_write_b16 v1, v3 offset:13376
	v_mul_f32_e32 v3, v2, v32
	v_cvt_pk_bf16_f32 v3, v3, s0
	ds_write_b16 v1, v3 offset:13440
	v_rcp_f32_e32 v3, v81
	v_mul_f32_e32 v2, v2, v16
	v_cvt_pk_bf16_f32 v2, v2, s0
	ds_write_b16 v1, v2 offset:13504
	v_mul_f32_e32 v2, v3, v65
	v_cvt_pk_bf16_f32 v2, v2, s0
	ds_write_b16 v1, v2 offset:13824
	v_mul_f32_e32 v2, v3, v49
	v_cvt_pk_bf16_f32 v2, v2, s0
	ds_write_b16 v1, v2 offset:13888
	v_mul_f32_e32 v2, v3, v33
	v_cvt_pk_bf16_f32 v2, v2, s0
	v_mul_f32_e32 v50, v66, v50
	v_mul_f32_e32 v34, v66, v34
	ds_write_b16 v1, v2 offset:13952
	v_mul_f32_e32 v2, v3, v17
	v_cvt_pk_bf16_f32 v50, v50, s0
	v_cvt_pk_bf16_f32 v34, v34, s0
	v_cvt_pk_bf16_f32 v2, v2, s0
	ds_write_b16 v1, v50
	ds_write_b16 v1, v34 offset:64
	ds_write_b16 v1, v2 offset:14016
	v_lshl_add_u32 v1, v0, 4, 0
	s_waitcnt lgkmcnt(0)
	s_barrier
	ds_read_b128 v[16:19], v1
	ds_read_b128 v[20:23], v1 offset:8192
	ds_read_b128 v[24:27], v1 offset:16384
	ds_read_b128 v[28:31], v1 offset:24576
	ds_read_b128 v[32:35], v1 offset:32768
	ds_read_b128 v[36:39], v1 offset:40960
	ds_read_b128 v[40:43], v1 offset:49152
	ds_read_b128 v[44:47], v1 offset:57344
	s_lshl_b64 s[2:3], s[6:7], 8
	s_add_u32 s2, s12, s2
	s_addc_u32 s3, s13, s3
	s_lshl_b32 s0, s8, 2
	s_add_u32 s0, s14, s0
	s_addc_u32 s1, s15, 0
	s_add_u32 s0, s0, s10
	s_addc_u32 s1, s1, s11
	s_mov_b32 s6, 0xda24260
	s_mov_b32 s7, 0xc0c0400
	s_mov_b32 s8, 0x4000c0c
	s_mov_b32 s9, 0x80808080
	v_lshlrev_b32_e32 v10, 3, v0
	v_lshrrev_b32_e32 v11, 3, v0
	s_waitcnt lgkmcnt(4)
	v_lshlrev_b32_e32 v64, 16, v16
	v_and_b32_e32 v65, 0xffff0000, v16
	v_lshlrev_b32_e32 v66, 16, v17
	v_and_b32_e32 v67, 0xffff0000, v17
	v_lshlrev_b32_e32 v68, 16, v18
	v_and_b32_e32 v69, 0xffff0000, v18
	v_lshlrev_b32_e32 v70, 16, v19
	v_and_b32_e32 v71, 0xffff0000, v19
	v_lshlrev_b32_e32 v76, 16, v20
	v_and_b32_e32 v77, 0xffff0000, v20
	v_lshlrev_b32_e32 v78, 16, v21
	v_and_b32_e32 v79, 0xffff0000, v21
	v_lshlrev_b32_e32 v80, 16, v22
	v_and_b32_e32 v81, 0xffff0000, v22
	v_lshlrev_b32_e32 v82, 16, v23
	v_and_b32_e32 v83, 0xffff0000, v23
	v_lshlrev_b32_e32 v88, 16, v24
	v_and_b32_e32 v89, 0xffff0000, v24
	v_lshlrev_b32_e32 v90, 16, v25
	v_and_b32_e32 v91, 0xffff0000, v25
	v_lshlrev_b32_e32 v92, 16, v26
	v_and_b32_e32 v93, 0xffff0000, v26
	v_lshlrev_b32_e32 v94, 16, v27
	v_and_b32_e32 v95, 0xffff0000, v27
	v_lshlrev_b32_e32 v100, 16, v28
	v_and_b32_e32 v101, 0xffff0000, v28
	v_lshlrev_b32_e32 v102, 16, v29
	v_and_b32_e32 v103, 0xffff0000, v29
	v_lshlrev_b32_e32 v104, 16, v30
	v_and_b32_e32 v105, 0xffff0000, v30
	v_lshlrev_b32_e32 v106, 16, v31
	v_and_b32_e32 v107, 0xffff0000, v31
	v_max_f32_e64 v48, |v64|, |v65|
	v_max_f32_e64 v49, |v76|, |v77|
	v_max_f32_e64 v50, |v88|, |v89|
	v_max_f32_e64 v51, |v100|, |v101|
	v_max3_f32 v48, v48, |v66|, |v67|
	v_max3_f32 v49, v49, |v78|, |v79|
	v_max3_f32 v50, v50, |v90|, |v91|
	v_max3_f32 v51, v51, |v102|, |v103|
	v_max3_f32 v48, v48, |v68|, |v69|
	v_max3_f32 v49, v49, |v80|, |v81|
	v_max3_f32 v50, v50, |v92|, |v93|
	v_max3_f32 v51, v51, |v104|, |v105|
	v_max3_f32 v48, v48, |v70|, |v71|
	v_max3_f32 v49, v49, |v82|, |v83|
	v_max3_f32 v50, v50, |v94|, |v95|
	v_max3_f32 v51, v51, |v106|, |v107|
	v_max_f32_dpp v48, v48, v48 quad_perm:[1,0,3,2] row_mask:0xf bank_mask:0xf
	v_max_f32_dpp v49, v49, v49 quad_perm:[1,0,3,2] row_mask:0xf bank_mask:0xf
	v_max_f32_dpp v50, v50, v50 quad_perm:[1,0,3,2] row_mask:0xf bank_mask:0xf
	v_max_f32_dpp v51, v51, v51 quad_perm:[1,0,3,2] row_mask:0xf bank_mask:0xf
	v_max_f32_dpp v48, v48, v48 quad_perm:[2,3,0,1] row_mask:0xf bank_mask:0xf
	v_max_f32_dpp v49, v49, v49 quad_perm:[2,3,0,1] row_mask:0xf bank_mask:0xf
	v_max_f32_dpp v50, v50, v50 quad_perm:[2,3,0,1] row_mask:0xf bank_mask:0xf
	v_max_f32_dpp v51, v51, v51 quad_perm:[2,3,0,1] row_mask:0xf bank_mask:0xf
	v_max_f32_dpp v48, v48, v48 row_half_mirror row_mask:0xf bank_mask:0xf
	v_max_f32_dpp v49, v49, v49 row_half_mirror row_mask:0xf bank_mask:0xf
	v_max_f32_dpp v50, v50, v50 row_half_mirror row_mask:0xf bank_mask:0xf
	v_max_f32_dpp v51, v51, v51 row_half_mirror row_mask:0xf bank_mask:0xf
	v_max_f32_dpp v48, v48, v48 row_mirror row_mask:0xf bank_mask:0xf
	v_max_f32_dpp v49, v49, v49 row_mirror row_mask:0xf bank_mask:0xf
	v_max_f32_dpp v50, v50, v50 row_mirror row_mask:0xf bank_mask:0xf
	v_max_f32_dpp v51, v51, v51 row_mirror row_mask:0xf bank_mask:0xf
	v_mov_b32_e32 v72, v48
	v_mov_b32_e32 v84, v49
	v_mov_b32_e32 v96, v50
	v_mov_b32_e32 v108, v51
	v_permlane16_swap_b32_e32 v72, v48
	v_permlane16_swap_b32_e32 v84, v49
	v_permlane16_swap_b32_e32 v96, v50
	v_permlane16_swap_b32_e32 v108, v51
	v_max_f32_e32 v48, v72, v48
	v_max_f32_e32 v49, v84, v49
	v_max_f32_e32 v50, v96, v50
	v_max_f32_e32 v51, v108, v51
	v_max_f32_e32 v48, s6, v48
	v_max_f32_e32 v49, s6, v49
	v_max_f32_e32 v50, s6, v50
	v_max_f32_e32 v51, s6, v51
	v_rcp_f32_e32 v73, v48
	v_rcp_f32_e32 v85, v49
	v_rcp_f32_e32 v97, v50
	v_rcp_f32_e32 v109, v51
	v_mul_f32_e32 v73, 0x42fe0000, v73
	v_mul_f32_e32 v85, 0x42fe0000, v85
	v_mul_f32_e32 v97, 0x42fe0000, v97
	v_mul_f32_e32 v109, 0x42fe0000, v109
	v_mul_f32_e32 v73, 0x3f7fffff, v73
	v_mul_f32_e32 v85, 0x3f7fffff, v85
	v_mul_f32_e32 v97, 0x3f7fffff, v97
	v_mul_f32_e32 v109, 0x3f7fffff, v109
	v_fmaak_f32 v64, v64, v73, 0x4b400000
	v_fmaak_f32 v65, v65, v73, 0x4b400000
	v_fmaak_f32 v66, v66, v73, 0x4b400000
	v_fmaak_f32 v67, v67, v73, 0x4b400000
	v_fmaak_f32 v68, v68, v73, 0x4b400000
	v_fmaak_f32 v69, v69, v73, 0x4b400000
	v_fmaak_f32 v70, v70, v73, 0x4b400000
	v_fmaak_f32 v71, v71, v73, 0x4b400000
	v_fmaak_f32 v76, v76, v85, 0x4b400000
	v_fmaak_f32 v77, v77, v85, 0x4b400000
	v_fmaak_f32 v78, v78, v85, 0x4b400000
	v_fmaak_f32 v79, v79, v85, 0x4b400000
	v_fmaak_f32 v80, v80, v85, 0x4b400000
	v_fmaak_f32 v81, v81, v85, 0x4b400000
	v_fmaak_f32 v82, v82, v85, 0x4b400000
	v_fmaak_f32 v83, v83, v85, 0x4b400000
	v_fmaak_f32 v88, v88, v97, 0x4b400000
	v_fmaak_f32 v89, v89, v97, 0x4b400000
	v_fmaak_f32 v90, v90, v97, 0x4b400000
	v_fmaak_f32 v91, v91, v97, 0x4b400000
	v_fmaak_f32 v92, v92, v97, 0x4b400000
	v_fmaak_f32 v93, v93, v97, 0x4b400000
	v_fmaak_f32 v94, v94, v97, 0x4b400000
	v_fmaak_f32 v95, v95, v97, 0x4b400000
	v_fmaak_f32 v100, v100, v109, 0x4b400000
	v_fmaak_f32 v101, v101, v109, 0x4b400000
	v_fmaak_f32 v102, v102, v109, 0x4b400000
	v_fmaak_f32 v103, v103, v109, 0x4b400000
	v_fmaak_f32 v104, v104, v109, 0x4b400000
	v_fmaak_f32 v105, v105, v109, 0x4b400000
	v_fmaak_f32 v106, v106, v109, 0x4b400000
	v_fmaak_f32 v107, v107, v109, 0x4b400000
	v_perm_b32 v64, v65, v64, s7
	v_perm_b32 v66, v67, v66, s8
	v_perm_b32 v68, v69, v68, s7
	v_perm_b32 v70, v71, v70, s8
	v_perm_b32 v76, v77, v76, s7
	v_perm_b32 v78, v79, v78, s8
	v_perm_b32 v80, v81, v80, s7
	v_perm_b32 v82, v83, v82, s8
	v_perm_b32 v88, v89, v88, s7
	v_perm_b32 v90, v91, v90, s8
	v_perm_b32 v92, v93, v92, s7
	v_perm_b32 v94, v95, v94, s8
	v_perm_b32 v100, v101, v100, s7
	v_perm_b32 v102, v103, v102, s8
	v_perm_b32 v104, v105, v104, s7
	v_perm_b32 v106, v107, v106, s8
	v_bitop3_b32 v64, v64, s9, v66 bitop3:0x36
	v_bitop3_b32 v65, v68, s9, v70 bitop3:0x36
	v_bitop3_b32 v76, v76, s9, v78 bitop3:0x36
	v_bitop3_b32 v77, v80, s9, v82 bitop3:0x36
	v_bitop3_b32 v88, v88, s9, v90 bitop3:0x36
	v_bitop3_b32 v89, v92, s9, v94 bitop3:0x36
	v_bitop3_b32 v100, v100, s9, v102 bitop3:0x36
	v_bitop3_b32 v101, v104, s9, v106 bitop3:0x36
	global_store_dwordx2 v10, v[64:65], s[2:3]
	v_add_u32_e32 v86, 4096, v10
	global_store_dwordx2 v86, v[76:77], s[2:3]
	v_add_u32_e32 v98, 8192, v10
	global_store_dwordx2 v98, v[88:89], s[2:3]
	v_add_u32_e32 v110, 12288, v10
	global_store_dwordx2 v110, v[100:101], s[2:3]
	s_waitcnt lgkmcnt(0)
	v_lshlrev_b32_e32 v64, 16, v32
	v_and_b32_e32 v65, 0xffff0000, v32
	v_lshlrev_b32_e32 v66, 16, v33
	v_and_b32_e32 v67, 0xffff0000, v33
	v_lshlrev_b32_e32 v68, 16, v34
	v_and_b32_e32 v69, 0xffff0000, v34
	v_lshlrev_b32_e32 v70, 16, v35
	v_and_b32_e32 v71, 0xffff0000, v35
	v_lshlrev_b32_e32 v76, 16, v36
	v_and_b32_e32 v77, 0xffff0000, v36
	v_lshlrev_b32_e32 v78, 16, v37
	v_and_b32_e32 v79, 0xffff0000, v37
	v_lshlrev_b32_e32 v80, 16, v38
	v_and_b32_e32 v81, 0xffff0000, v38
	v_lshlrev_b32_e32 v82, 16, v39
	v_and_b32_e32 v83, 0xffff0000, v39
	v_lshlrev_b32_e32 v88, 16, v40
	v_and_b32_e32 v89, 0xffff0000, v40
	v_lshlrev_b32_e32 v90, 16, v41
	v_and_b32_e32 v91, 0xffff0000, v41
	v_lshlrev_b32_e32 v92, 16, v42
	v_and_b32_e32 v93, 0xffff0000, v42
	v_lshlrev_b32_e32 v94, 16, v43
	v_and_b32_e32 v95, 0xffff0000, v43
	v_lshlrev_b32_e32 v100, 16, v44
	v_and_b32_e32 v101, 0xffff0000, v44
	v_lshlrev_b32_e32 v102, 16, v45
	v_and_b32_e32 v103, 0xffff0000, v45
	v_lshlrev_b32_e32 v104, 16, v46
	v_and_b32_e32 v105, 0xffff0000, v46
	v_lshlrev_b32_e32 v106, 16, v47
	v_and_b32_e32 v107, 0xffff0000, v47
	v_max_f32_e64 v52, |v64|, |v65|
	v_max_f32_e64 v53, |v76|, |v77|
	v_max_f32_e64 v54, |v88|, |v89|
	v_max_f32_e64 v55, |v100|, |v101|
	v_max3_f32 v52, v52, |v66|, |v67|
	v_max3_f32 v53, v53, |v78|, |v79|
	v_max3_f32 v54, v54, |v90|, |v91|
	v_max3_f32 v55, v55, |v102|, |v103|
	v_max3_f32 v52, v52, |v68|, |v69|
	v_max3_f32 v53, v53, |v80|, |v81|
	v_max3_f32 v54, v54, |v92|, |v93|
	v_max3_f32 v55, v55, |v104|, |v105|
	v_max3_f32 v52, v52, |v70|, |v71|
	v_max3_f32 v53, v53, |v82|, |v83|
	v_max3_f32 v54, v54, |v94|, |v95|
	v_max3_f32 v55, v55, |v106|, |v107|
	v_max_f32_dpp v52, v52, v52 quad_perm:[1,0,3,2] row_mask:0xf bank_mask:0xf
	v_max_f32_dpp v53, v53, v53 quad_perm:[1,0,3,2] row_mask:0xf bank_mask:0xf
	v_max_f32_dpp v54, v54, v54 quad_perm:[1,0,3,2] row_mask:0xf bank_mask:0xf
	v_max_f32_dpp v55, v55, v55 quad_perm:[1,0,3,2] row_mask:0xf bank_mask:0xf
	v_max_f32_dpp v52, v52, v52 quad_perm:[2,3,0,1] row_mask:0xf bank_mask:0xf
	v_max_f32_dpp v53, v53, v53 quad_perm:[2,3,0,1] row_mask:0xf bank_mask:0xf
	v_max_f32_dpp v54, v54, v54 quad_perm:[2,3,0,1] row_mask:0xf bank_mask:0xf
	v_max_f32_dpp v55, v55, v55 quad_perm:[2,3,0,1] row_mask:0xf bank_mask:0xf
	v_max_f32_dpp v52, v52, v52 row_half_mirror row_mask:0xf bank_mask:0xf
	v_max_f32_dpp v53, v53, v53 row_half_mirror row_mask:0xf bank_mask:0xf
	v_max_f32_dpp v54, v54, v54 row_half_mirror row_mask:0xf bank_mask:0xf
	v_max_f32_dpp v55, v55, v55 row_half_mirror row_mask:0xf bank_mask:0xf
	v_max_f32_dpp v52, v52, v52 row_mirror row_mask:0xf bank_mask:0xf
	v_max_f32_dpp v53, v53, v53 row_mirror row_mask:0xf bank_mask:0xf
	v_max_f32_dpp v54, v54, v54 row_mirror row_mask:0xf bank_mask:0xf
	v_max_f32_dpp v55, v55, v55 row_mirror row_mask:0xf bank_mask:0xf
	v_mov_b32_e32 v72, v52
	v_mov_b32_e32 v84, v53
	v_mov_b32_e32 v96, v54
	v_mov_b32_e32 v108, v55
	v_permlane16_swap_b32_e32 v72, v52
	v_permlane16_swap_b32_e32 v84, v53
	v_permlane16_swap_b32_e32 v96, v54
	v_permlane16_swap_b32_e32 v108, v55
	v_max_f32_e32 v52, v72, v52
	v_max_f32_e32 v53, v84, v53
	v_max_f32_e32 v54, v96, v54
	v_max_f32_e32 v55, v108, v55
	v_max_f32_e32 v52, s6, v52
	v_max_f32_e32 v53, s6, v53
	v_max_f32_e32 v54, s6, v54
	v_max_f32_e32 v55, s6, v55
	v_rcp_f32_e32 v73, v52
	v_rcp_f32_e32 v85, v53
	v_rcp_f32_e32 v97, v54
	v_rcp_f32_e32 v109, v55
	v_mul_f32_e32 v73, 0x42fe0000, v73
	v_mul_f32_e32 v85, 0x42fe0000, v85
	v_mul_f32_e32 v97, 0x42fe0000, v97
	v_mul_f32_e32 v109, 0x42fe0000, v109
	v_mul_f32_e32 v73, 0x3f7fffff, v73
	v_mul_f32_e32 v85, 0x3f7fffff, v85
	v_mul_f32_e32 v97, 0x3f7fffff, v97
	v_mul_f32_e32 v109, 0x3f7fffff, v109
	v_fmaak_f32 v64, v64, v73, 0x4b400000
	v_fmaak_f32 v65, v65, v73, 0x4b400000
	v_fmaak_f32 v66, v66, v73, 0x4b400000
	v_fmaak_f32 v67, v67, v73, 0x4b400000
	v_fmaak_f32 v68, v68, v73, 0x4b400000
	v_fmaak_f32 v69, v69, v73, 0x4b400000
	v_fmaak_f32 v70, v70, v73, 0x4b400000
	v_fmaak_f32 v71, v71, v73, 0x4b400000
	v_fmaak_f32 v76, v76, v85, 0x4b400000
	v_fmaak_f32 v77, v77, v85, 0x4b400000
	v_fmaak_f32 v78, v78, v85, 0x4b400000
	v_fmaak_f32 v79, v79, v85, 0x4b400000
	v_fmaak_f32 v80, v80, v85, 0x4b400000
	v_fmaak_f32 v81, v81, v85, 0x4b400000
	v_fmaak_f32 v82, v82, v85, 0x4b400000
	v_fmaak_f32 v83, v83, v85, 0x4b400000
	v_fmaak_f32 v88, v88, v97, 0x4b400000
	v_fmaak_f32 v89, v89, v97, 0x4b400000
	v_fmaak_f32 v90, v90, v97, 0x4b400000
	v_fmaak_f32 v91, v91, v97, 0x4b400000
	v_fmaak_f32 v92, v92, v97, 0x4b400000
	v_fmaak_f32 v93, v93, v97, 0x4b400000
	v_fmaak_f32 v94, v94, v97, 0x4b400000
	v_fmaak_f32 v95, v95, v97, 0x4b400000
	v_fmaak_f32 v100, v100, v109, 0x4b400000
	v_fmaak_f32 v101, v101, v109, 0x4b400000
	v_fmaak_f32 v102, v102, v109, 0x4b400000
	v_fmaak_f32 v103, v103, v109, 0x4b400000
	v_fmaak_f32 v104, v104, v109, 0x4b400000
	v_fmaak_f32 v105, v105, v109, 0x4b400000
	v_fmaak_f32 v106, v106, v109, 0x4b400000
	v_fmaak_f32 v107, v107, v109, 0x4b400000
	v_perm_b32 v64, v65, v64, s7
	v_perm_b32 v66, v67, v66, s8
	v_perm_b32 v68, v69, v68, s7
	v_perm_b32 v70, v71, v70, s8
	v_perm_b32 v76, v77, v76, s7
	v_perm_b32 v78, v79, v78, s8
	v_perm_b32 v80, v81, v80, s7
	v_perm_b32 v82, v83, v82, s8
	v_perm_b32 v88, v89, v88, s7
	v_perm_b32 v90, v91, v90, s8
	v_perm_b32 v92, v93, v92, s7
	v_perm_b32 v94, v95, v94, s8
	v_perm_b32 v100, v101, v100, s7
	v_perm_b32 v102, v103, v102, s8
	v_perm_b32 v104, v105, v104, s7
	v_perm_b32 v106, v107, v106, s8
	v_bitop3_b32 v64, v64, s9, v66 bitop3:0x36
	v_bitop3_b32 v65, v68, s9, v70 bitop3:0x36
	v_bitop3_b32 v76, v76, s9, v78 bitop3:0x36
	v_bitop3_b32 v77, v80, s9, v82 bitop3:0x36
	v_bitop3_b32 v88, v88, s9, v90 bitop3:0x36
	v_bitop3_b32 v89, v92, s9, v94 bitop3:0x36
	v_bitop3_b32 v100, v100, s9, v102 bitop3:0x36
	v_bitop3_b32 v101, v104, s9, v106 bitop3:0x36
	v_add_u32_e32 v74, 16384, v10
	global_store_dwordx2 v74, v[64:65], s[2:3]
	v_add_u32_e32 v86, 20480, v10
	global_store_dwordx2 v86, v[76:77], s[2:3]
	v_add_u32_e32 v98, 24576, v10
	global_store_dwordx2 v98, v[88:89], s[2:3]
	v_add_u32_e32 v110, 28672, v10
	global_store_dwordx2 v110, v[100:101], s[2:3]
	s_and_saveexec_b64 s[4:5], vcc
	v_mul_f32_e32 v48, 0x3c010204, v48
	v_mul_f32_e32 v49, 0x3c010204, v49
	v_mul_f32_e32 v50, 0x3c010204, v50
	v_mul_f32_e32 v51, 0x3c010204, v51
	v_mul_f32_e32 v52, 0x3c010204, v52
	v_mul_f32_e32 v53, 0x3c010204, v53
	v_mul_f32_e32 v54, 0x3c010204, v54
	v_mul_f32_e32 v55, 0x3c010204, v55
	global_store_dword v11, v48, s[0:1]
	global_store_dword v11, v49, s[0:1] offset:64
	global_store_dword v11, v50, s[0:1] offset:128
	global_store_dword v11, v51, s[0:1] offset:192
	global_store_dword v11, v52, s[0:1] offset:256
	global_store_dword v11, v53, s[0:1] offset:320
	global_store_dword v11, v54, s[0:1] offset:384
	global_store_dword v11, v55, s[0:1] offset:448
	s_endpgm
